# causal attention body first half-step: waves 4-7 also run mask+partialSM before the P.V MFMA block (register-independent), so the whole half-step alternates MFMA/VALU between the two wave groups
# speedup vs baseline: 1.0056x; 1.0056x over previous
.Lsw0_done:
	v_add_u32_e32 v177, s85, v167
	v_add_u32_e32 v138, 1, v177
	v_add_u32_e32 v140, 33, v177
	v_mad_i64_i32 v[130:131], s[2:3], v138, s71, v[172:173]
	v_mad_i64_i32 v[134:135], s[2:3], v140, s71, v[172:173]
	v_mad_i64_i32 v[138:139], s[2:3], v138, s71, v[174:175]
	v_mad_i64_i32 v[142:143], s[2:3], v140, s71, v[174:175]
	global_load_dwordx4 v[130:133], v[130:131], off
	s_nop 0
	global_load_dwordx4 v[134:137], v[134:135], off
	s_nop 0
	global_load_dwordx4 v[138:141], v[138:139], off
	s_nop 0
	global_load_dwordx4 v[142:145], v[142:143], off
	v_readlane_b32 vcc_lo, v255, 63
	s_mov_b32 vcc_hi, 0
	s_cbranch_vccnz .Lpv_L2hs1pv_S
.Lpv_L2hs1pv_P:
	s_setprio 1
	ds_read_b64_tr_b16 v[210:211], v188 offset:0
	ds_read_b64_tr_b16 v[212:213], v188 offset:0x800
	ds_read_b64_tr_b16 v[214:215], v188 offset:0x1000
	ds_read_b64_tr_b16 v[216:217], v188 offset:0x1800
	ds_read_b64_tr_b16 v[218:219], v188 offset:0x2000
	ds_read_b64_tr_b16 v[220:221], v188 offset:0x2800
	ds_read_b64_tr_b16 v[222:223], v188 offset:0x3000
	ds_read_b64_tr_b16 v[224:225], v188 offset:0x3800
	s_waitcnt lgkmcnt(0)
	s_nop 0
	v_mfma_f32_32x32x16_bf16 v[34:49], v[148:151], v[210:213], v[34:49]
	ds_read_b64_tr_b16 v[210:211], v188 offset:0x200
	ds_read_b64_tr_b16 v[212:213], v188 offset:0xa00
	v_mfma_f32_32x32x16_bf16 v[34:49], v[152:155], v[214:217], v[34:49]
	ds_read_b64_tr_b16 v[214:215], v188 offset:0x1200
	ds_read_b64_tr_b16 v[216:217], v188 offset:0x1a00
	v_mfma_f32_32x32x16_bf16 v[34:49], v[156:159], v[218:221], v[34:49]
	ds_read_b64_tr_b16 v[218:219], v188 offset:0x2200
	ds_read_b64_tr_b16 v[220:221], v188 offset:0x2a00
	v_mfma_f32_32x32x16_bf16 v[34:49], v[206:209], v[222:225], v[34:49]
	ds_read_b64_tr_b16 v[222:223], v188 offset:0x3200
	ds_read_b64_tr_b16 v[224:225], v188 offset:0x3a00
	s_waitcnt lgkmcnt(0)
	v_mfma_f32_32x32x16_bf16 v[50:65], v[148:151], v[210:213], v[50:65]
	ds_read_b64_tr_b16 v[210:211], v188 offset:0x400
	ds_read_b64_tr_b16 v[212:213], v188 offset:0xc00
	v_mfma_f32_32x32x16_bf16 v[50:65], v[152:155], v[214:217], v[50:65]
	ds_read_b64_tr_b16 v[214:215], v188 offset:0x1400
	ds_read_b64_tr_b16 v[216:217], v188 offset:0x1c00
	v_mfma_f32_32x32x16_bf16 v[50:65], v[156:159], v[218:221], v[50:65]
	ds_read_b64_tr_b16 v[218:219], v188 offset:0x2400
	ds_read_b64_tr_b16 v[220:221], v188 offset:0x2c00
	v_mfma_f32_32x32x16_bf16 v[50:65], v[206:209], v[222:225], v[50:65]
	ds_read_b64_tr_b16 v[222:223], v188 offset:0x3400
	ds_read_b64_tr_b16 v[224:225], v188 offset:0x3c00
	s_waitcnt lgkmcnt(0)
	v_mfma_f32_32x32x16_bf16 v[18:33], v[148:151], v[210:213], v[18:33]
	ds_read_b64_tr_b16 v[210:211], v188 offset:0x600
	ds_read_b64_tr_b16 v[212:213], v188 offset:0xe00
	v_mfma_f32_32x32x16_bf16 v[18:33], v[152:155], v[214:217], v[18:33]
	ds_read_b64_tr_b16 v[214:215], v188 offset:0x1600
	ds_read_b64_tr_b16 v[216:217], v188 offset:0x1e00
	v_mfma_f32_32x32x16_bf16 v[18:33], v[156:159], v[218:221], v[18:33]
	ds_read_b64_tr_b16 v[218:219], v188 offset:0x2600
	ds_read_b64_tr_b16 v[220:221], v188 offset:0x2e00
	v_mfma_f32_32x32x16_bf16 v[18:33], v[206:209], v[222:225], v[18:33]
	ds_read_b64_tr_b16 v[222:223], v188 offset:0x3600
	ds_read_b64_tr_b16 v[224:225], v188 offset:0x3e00
	s_waitcnt lgkmcnt(0)
	v_mfma_f32_32x32x16_bf16 v[2:17], v[148:151], v[210:213], v[2:17]
	v_mfma_f32_32x32x16_bf16 v[2:17], v[152:155], v[214:217], v[2:17]
	v_mfma_f32_32x32x16_bf16 v[2:17], v[156:159], v[218:221], v[2:17]
	v_mfma_f32_32x32x16_bf16 v[2:17], v[206:209], v[222:225], v[2:17]
	s_setprio 0
	v_readlane_b32 vcc_lo, v255, 63
	s_mov_b32 vcc_hi, 0
	s_cbranch_vccnz .Lpv_L2hs1pv_E
.Lpv_L2hs1pv_S:
	s_cmp_le_i32 s85, s78
	s_cbranch_scc1 .LBB0_1262
	v_cmp_gt_i32_e64 s[60:61], 26, v146
	v_cmp_gt_i32_e64 s[62:63], 27, v146
	v_cmp_gt_i32_e64 s[58:59], 25, v146
	s_and_b64 s[60:61], s[62:63], s[60:61]
	v_cmp_gt_i32_e64 s[56:57], 24, v146
	s_and_b64 s[58:59], s[60:61], s[58:59]
	v_cmp_gt_i32_e64 s[54:55], 19, v146
	s_and_b64 s[56:57], s[58:59], s[56:57]
	v_cmp_gt_i32_e64 s[52:53], 18, v146
	s_and_b64 s[54:55], s[56:57], s[54:55]
	v_cmp_gt_i32_e64 s[50:51], 17, v146
	s_and_b64 s[52:53], s[54:55], s[52:53]
	v_cmp_gt_i32_e64 s[48:49], 16, v146
	s_and_b64 s[50:51], s[52:53], s[50:51]
	v_cmp_gt_i32_e64 s[46:47], 11, v146
	s_and_b64 s[48:49], s[50:51], s[48:49]
	v_cmp_gt_i32_e64 s[44:45], 10, v146
	s_and_b64 s[46:47], s[48:49], s[46:47]
	v_cmp_gt_i32_e64 s[42:43], 9, v146
	s_and_b64 s[44:45], s[46:47], s[44:45]
	v_cmp_gt_i32_e64 s[40:41], 8, v146
	s_and_b64 s[42:43], s[44:45], s[42:43]
	v_cmp_gt_i32_e64 s[38:39], 3, v146
	s_and_b64 s[40:41], s[42:43], s[40:41]
	v_cmp_gt_i32_e64 s[36:37], 2, v146
	s_and_b64 s[38:39], s[40:41], s[38:39]
	v_cmp_gt_i32_e64 s[34:35], 1, v146
	s_and_b64 s[36:37], s[38:39], s[36:37]
	v_cmp_gt_i32_e64 s[30:31], 0, v146
	s_and_b64 s[34:35], s[36:37], s[34:35]
	s_and_b64 s[30:31], s[34:35], s[30:31]
	v_cmp_gt_i32_e64 s[28:29], 58, v146
	v_cndmask_b32_e64 v66, v66, v243, s[30:31]
	v_cmp_gt_i32_e64 s[30:31], 59, v146
	v_cmp_gt_i32_e64 s[26:27], 57, v146
	s_and_b64 s[28:29], s[30:31], s[28:29]
	v_cmp_gt_i32_e64 s[24:25], 56, v146
	s_and_b64 s[26:27], s[28:29], s[26:27]
	v_cmp_gt_i32_e64 s[22:23], 51, v146
	s_and_b64 s[24:25], s[26:27], s[24:25]
	v_cmp_gt_i32_e64 s[20:21], 50, v146
	s_and_b64 s[22:23], s[24:25], s[22:23]
	v_cmp_gt_i32_e64 s[18:19], 49, v146
	s_and_b64 s[20:21], s[22:23], s[20:21]
	v_cmp_gt_i32_e64 s[16:17], 48, v146
	s_and_b64 s[18:19], s[20:21], s[18:19]
	v_cmp_gt_i32_e64 s[14:15], 43, v146
	s_and_b64 s[16:17], s[18:19], s[16:17]
	v_cmp_gt_i32_e64 s[12:13], 42, v146
	s_and_b64 s[14:15], s[16:17], s[14:15]
	v_cmp_gt_i32_e64 s[10:11], 41, v146
	s_and_b64 s[12:13], s[14:15], s[12:13]
	v_cmp_gt_i32_e64 s[8:9], 40, v146
	s_and_b64 s[10:11], s[12:13], s[10:11]
	v_cmp_gt_i32_e64 s[6:7], 35, v146
	s_and_b64 s[8:9], s[10:11], s[8:9]
	v_cmp_gt_i32_e64 s[4:5], 34, v146
	s_and_b64 s[6:7], s[8:9], s[6:7]
	v_cmp_gt_i32_e64 s[2:3], 33, v146
	s_and_b64 s[4:5], s[6:7], s[4:5]
	v_cmp_gt_i32_e32 vcc, 32, v146
	s_and_b64 s[2:3], s[4:5], s[2:3]
	v_cndmask_b32_e64 v81, v81, v243, s[62:63]
	s_mov_b32 s62, 0x41200000
	v_cndmask_b32_e64 v80, v80, v243, s[60:61]
	s_mov_b32 s60, 2.0
	v_cndmask_b32_e64 v79, v79, v243, s[58:59]
	s_mov_b32 s58, 0x41800000
	s_and_b64 vcc, s[2:3], vcc
	s_mov_b32 s63, 0x41300000
	s_mov_b32 s61, 0x40400000
	s_mov_b32 s59, 0x41880000
	v_cndmask_b32_e64 v78, v78, v243, s[56:57]
	v_cndmask_b32_e64 v77, v77, v243, s[54:55]
	v_cndmask_b32_e64 v76, v76, v243, s[52:53]
	v_cndmask_b32_e64 v75, v75, v243, s[50:51]
	v_cndmask_b32_e64 v74, v74, v243, s[48:49]
	v_cndmask_b32_e64 v73, v73, v243, s[46:47]
	v_cndmask_b32_e64 v72, v72, v243, s[44:45]
	v_cndmask_b32_e64 v71, v71, v243, s[42:43]
	v_cndmask_b32_e64 v70, v70, v243, s[40:41]
	v_cndmask_b32_e64 v69, v69, v243, s[38:39]
	v_cndmask_b32_e64 v68, v68, v243, s[36:37]
	v_cndmask_b32_e64 v67, v67, v243, s[34:35]
	v_cndmask_b32_e64 v97, v97, v243, s[30:31]
	v_cndmask_b32_e64 v96, v96, v243, s[28:29]
	v_cndmask_b32_e64 v95, v95, v243, s[26:27]
	v_cndmask_b32_e64 v94, v94, v243, s[24:25]
	v_cndmask_b32_e64 v93, v93, v243, s[22:23]
	v_cndmask_b32_e64 v92, v92, v243, s[20:21]
	v_cndmask_b32_e64 v91, v91, v243, s[18:19]
	v_cndmask_b32_e64 v90, v90, v243, s[16:17]
	v_cndmask_b32_e64 v89, v89, v243, s[14:15]
	v_cndmask_b32_e64 v88, v88, v243, s[12:13]
	v_cndmask_b32_e64 v87, v87, v243, s[10:11]
	v_cndmask_b32_e64 v86, v86, v243, s[8:9]
	v_cndmask_b32_e64 v85, v85, v243, s[6:7]
	v_cndmask_b32_e64 v84, v84, v243, s[4:5]
	v_cndmask_b32_e64 v83, v83, v243, s[2:3]
	v_cndmask_b32_e32 v82, v82, v243, vcc
.LBB0_1262:
	v_max_f32_e32 v146, v67, v67
	v_max_f32_e32 v147, v66, v66
	v_max_f32_e32 v146, v147, v146
	v_max3_f32 v146, v146, v68, v69
	v_max3_f32 v146, v146, v70, v71
	v_max3_f32 v146, v146, v72, v73
	v_max3_f32 v146, v146, v74, v75
	v_max3_f32 v146, v146, v76, v77
	v_max3_f32 v146, v146, v78, v79
	v_max3_f32 v146, v146, v80, v81
	v_max3_f32 v146, v146, v82, v83
	v_max3_f32 v146, v146, v84, v85
	v_max3_f32 v146, v146, v86, v87
	v_max3_f32 v146, v146, v88, v89
	v_max3_f32 v146, v146, v90, v91
	v_max3_f32 v146, v146, v92, v93
	v_max3_f32 v146, v146, v94, v95
	v_max3_f32 v146, v146, v96, v97
	v_mov_b32_e32 v147, v146
	s_nop 1
	v_permlane32_swap_b32_e32 v146, v147
	v_max_f32_e32 v147, v147, v147
	v_max_f32_e32 v146, v146, v146
	v_max_f32_e32 v146, v146, v147
	v_sub_f32_e32 v147, v146, v200
	v_mul_f32_e32 v147, 0x3db504f3, v147
	v_cmp_ge_f32_e32 vcc, s74, v147
	v_max_f32_e32 v147, v200, v200
	v_max_f32_e32 v146, v147, v146
	v_sub_f32_e32 v147, v200, v146
	v_mul_f32_e32 v147, 0x3e0293ee, v147
	v_exp_f32_e32 v147, v147
	s_cmp_eq_u64 vcc, exec
	v_readlane_b32 vcc_lo, v255, 63
	s_mov_b32 vcc_hi, 0
	s_cbranch_vccnz .Lpv_L2hs1pv_P
.Lpv_L2hs1pv_E:
	s_waitcnt lgkmcnt(0)
	s_barrier
	s_cselect_b64 s[2:3], -1, 0
	s_waitcnt vmcnt(0)
	v_cndmask_b32_e64 v207, v147, 1.0, s[2:3]
	v_cmp_gt_f32_e32 vcc, 1.0, v207
	s_waitcnt vmcnt(3)
	ds_write_b128 v194, v[130:133]
	s_waitcnt vmcnt(2)
	ds_write_b128 v194, v[134:137] offset:8192
	s_waitcnt vmcnt(1)
	ds_write_b128 v187, v[138:141] offset:32768
	s_waitcnt vmcnt(0)
	ds_write_b128 v187, v[142:145] offset:40960
	s_cbranch_vccz .LBB0_1266
	s_and_saveexec_b64 s[4:5], s[0:1]
	ds_write_b32 v190, v207 offset:128
	s_or_b64 exec, exec, s[4:5]
	s_waitcnt lgkmcnt(0)
	ds_read_b128 v[148:151], v189 offset:224
	ds_read_b128 v[152:155], v189 offset:192
	ds_read_b128 v[156:159], v189 offset:160
	ds_read_b128 v[208:211], v189 offset:128
	s_waitcnt lgkmcnt(3)
	v_pk_mul_f32 v[48:49], v[48:49], v[150:151]
	s_waitcnt lgkmcnt(2)
	v_pk_mul_f32 v[44:45], v[44:45], v[154:155]
	s_waitcnt lgkmcnt(1)
	v_pk_mul_f32 v[40:41], v[40:41], v[158:159]
	s_waitcnt lgkmcnt(0)
	v_pk_mul_f32 v[36:37], v[36:37], v[210:211]
	v_pk_mul_f32 v[46:47], v[46:47], v[148:149]
	v_pk_mul_f32 v[42:43], v[42:43], v[152:153]
	v_pk_mul_f32 v[38:39], v[38:39], v[156:157]
	v_pk_mul_f32 v[34:35], v[34:35], v[208:209]
	v_pk_mul_f32 v[64:65], v[64:65], v[150:151]
	v_pk_mul_f32 v[60:61], v[60:61], v[154:155]
	v_pk_mul_f32 v[56:57], v[56:57], v[158:159]
	v_pk_mul_f32 v[52:53], v[52:53], v[210:211]
	v_pk_mul_f32 v[62:63], v[62:63], v[148:149]
	v_pk_mul_f32 v[58:59], v[58:59], v[152:153]
	v_pk_mul_f32 v[54:55], v[54:55], v[156:157]
	v_pk_mul_f32 v[50:51], v[50:51], v[208:209]
	v_pk_mul_f32 v[32:33], v[32:33], v[150:151]
	v_pk_mul_f32 v[28:29], v[28:29], v[154:155]
	v_pk_mul_f32 v[24:25], v[24:25], v[158:159]
	v_pk_mul_f32 v[20:21], v[20:21], v[210:211]
	v_pk_mul_f32 v[30:31], v[30:31], v[148:149]
	v_pk_mul_f32 v[26:27], v[26:27], v[152:153]
	v_pk_mul_f32 v[22:23], v[22:23], v[156:157]
	v_pk_mul_f32 v[18:19], v[18:19], v[208:209]
	v_pk_mul_f32 v[16:17], v[16:17], v[150:151]
	v_pk_mul_f32 v[12:13], v[12:13], v[154:155]
	v_pk_mul_f32 v[8:9], v[8:9], v[158:159]
	v_pk_mul_f32 v[4:5], v[4:5], v[210:211]
	v_pk_mul_f32 v[14:15], v[14:15], v[148:149]
	v_pk_mul_f32 v[10:11], v[10:11], v[152:153]
	v_pk_mul_f32 v[6:7], v[6:7], v[156:157]
	v_pk_mul_f32 v[2:3], v[2:3], v[208:209]
